# edge span staged with 16-byte loads and ds_write_b128 (span start aligned down to two edges)
# speedup vs baseline: 1.0075x; 1.0075x over previous
_Z5k_hopILi0EEvPKiPK15HIP_vector_typeIiLj2EEPKS2_IjLj4EEPS6_S8_S8_PKfSB_Pf:
	s_lshr_b32 s3, s2, 3
	s_cmpk_gt_u32 s3, 156
	s_cbranch_scc1 .Lhq0_exit
	s_load_dwordx4 s[4:7], s[0:1], 0x0
	s_load_dwordx4 s[8:11], s[0:1], 0x10
	v_lshrrev_b32_e32 v2, 6, v0
	v_and_b32_e32 v3, 63, v0
	s_bfe_u32 s13, s2, 0x10002
	s_and_b32 s14, s2, 3
	v_readfirstlane_b32 s12, v2
	s_lshl_b32 s15, s3, 2
	s_add_i32 s15, s15, s12
	s_mul_i32 s15, s15, 40
	s_mul_i32 s16, s14, 25000
	s_add_i32 s15, s15, s16
	s_add_i32 s16, s16, 24960
	s_min_u32 s15, s15, s16
	s_mul_i32 s17, s13, 0x61a84
	s_waitcnt lgkmcnt(0)
	s_add_u32 s4, s4, s17
	s_addc_u32 s5, s5, 0
	s_mul_i32 s17, s13, 0x927c00
	s_add_u32 s6, s6, s17
	s_addc_u32 s7, s7, 0
	s_mul_i32 s17, s13, 0xc35000
	s_add_u32 s8, s8, s17
	s_addc_u32 s9, s9, 0
	s_add_u32 s10, s10, s17
	s_addc_u32 s11, s11, 0
	s_mul_i32 s28, s12, 6464
	s_mov_b32 s29, 0xffff80
	v_min_u32_e32 v4, 40, v3
	v_add_u32_e32 v4, s15, v4
	v_lshlrev_b32_e32 v4, 2, v4
	global_load_dword v5, v4, s[4:5]
	v_and_b32_e32 v1, 7, v0
	v_lshlrev_b32_e32 v1, 4, v1
	v_lshrrev_b32_e32 v2, 3, v3
	v_lshlrev_b32_e32 v2, 2, v2
	v_lshlrev_b32_e32 v4, 4, v3
	v_add_u32_e32 v6, s28, v4
	v_add_u32_e32 v7, 1, v3
	v_lshlrev_b32_e32 v7, 2, v7
	s_waitcnt vmcnt(0)
	v_readlane_b32 s18, v5, 0
	v_readlane_b32 s19, v5, 40
	ds_bpermute_b32 v8, v7, v5
	s_and_b32 s18, s18, -2
	s_sub_i32 s20, s19, s18
	s_lshl_b32 s21, s18, 3
	s_add_u32 s22, s6, s21
	s_addc_u32 s23, s7, 0
	s_add_u32 s24, s22, 0x1000
	s_addc_u32 s25, s23, 0
	s_cmpk_gt_i32 s20, 768
	s_cbranch_scc1 .Lhq0_staged
	global_load_dwordx4 v[56:59], v4, s[22:23] offset:0
	s_cmpk_le_i32 s20, 128
	s_cbranch_scc1 .Lhq0_staged
	global_load_dwordx4 v[60:63], v4, s[22:23] offset:1024
	s_cmpk_le_i32 s20, 256
	s_cbranch_scc1 .Lhq0_staged
	global_load_dwordx4 v[64:67], v4, s[22:23] offset:2048
	s_cmpk_le_i32 s20, 384
	s_cbranch_scc1 .Lhq0_staged
	global_load_dwordx4 v[68:71], v4, s[22:23] offset:3072
	s_cmpk_le_i32 s20, 512
	s_cbranch_scc1 .Lhq0_staged
	global_load_dwordx4 v[72:75], v4, s[24:25] offset:0
	s_cmpk_le_i32 s20, 640
	s_cbranch_scc1 .Lhq0_staged
	global_load_dwordx4 v[76:79], v4, s[24:25] offset:1024
.Lhq0_staged:
	s_waitcnt lgkmcnt(0)
	v_sub_u32_e32 v8, v8, v5
	v_lshlrev_b32_e32 v8, 6, v8
	v_sub_u32_e32 v9, 63, v3
	v_or_b32_e32 v8, v8, v9
	v_cmp_gt_u32_e32 vcc, 40, v3
	s_nop 1
	v_cndmask_b32_e32 v8, 0, v8, vcc
	v_lshlrev_b32_e32 v9, 2, v3
	v_add_u32_e32 v9, s28, v9
	ds_write_b32 v9, v8
	v_mov_b32_e32 v10, s28
	v_mov_b32_e32 v11, 0
	ds_read_b128 v[12:15], v10 offset:0
	ds_read_b128 v[16:19], v10 offset:16
	s_waitcnt lgkmcnt(0)
	v_sub_u32_e32 v20, v8, v12
	v_lshrrev_b32_e32 v20, 31, v20
	v_add_u32_e32 v11, v11, v20
	v_sub_u32_e32 v20, v8, v13
	v_lshrrev_b32_e32 v20, 31, v20
	v_add_u32_e32 v11, v11, v20
	v_sub_u32_e32 v20, v8, v14
	v_lshrrev_b32_e32 v20, 31, v20
	v_add_u32_e32 v11, v11, v20
	v_sub_u32_e32 v20, v8, v15
	v_lshrrev_b32_e32 v20, 31, v20
	v_add_u32_e32 v11, v11, v20
	v_sub_u32_e32 v20, v8, v16
	v_lshrrev_b32_e32 v20, 31, v20
	v_add_u32_e32 v11, v11, v20
	v_sub_u32_e32 v20, v8, v17
	v_lshrrev_b32_e32 v20, 31, v20
	v_add_u32_e32 v11, v11, v20
	v_sub_u32_e32 v20, v8, v18
	v_lshrrev_b32_e32 v20, 31, v20
	v_add_u32_e32 v11, v11, v20
	v_sub_u32_e32 v20, v8, v19
	v_lshrrev_b32_e32 v20, 31, v20
	v_add_u32_e32 v11, v11, v20
	ds_read_b128 v[12:15], v10 offset:32
	ds_read_b128 v[16:19], v10 offset:48
	s_waitcnt lgkmcnt(0)
	v_sub_u32_e32 v20, v8, v12
	v_lshrrev_b32_e32 v20, 31, v20
	v_add_u32_e32 v11, v11, v20
	v_sub_u32_e32 v20, v8, v13
	v_lshrrev_b32_e32 v20, 31, v20
	v_add_u32_e32 v11, v11, v20
	v_sub_u32_e32 v20, v8, v14
	v_lshrrev_b32_e32 v20, 31, v20
	v_add_u32_e32 v11, v11, v20
	v_sub_u32_e32 v20, v8, v15
	v_lshrrev_b32_e32 v20, 31, v20
	v_add_u32_e32 v11, v11, v20
	v_sub_u32_e32 v20, v8, v16
	v_lshrrev_b32_e32 v20, 31, v20
	v_add_u32_e32 v11, v11, v20
	v_sub_u32_e32 v20, v8, v17
	v_lshrrev_b32_e32 v20, 31, v20
	v_add_u32_e32 v11, v11, v20
	v_sub_u32_e32 v20, v8, v18
	v_lshrrev_b32_e32 v20, 31, v20
	v_add_u32_e32 v11, v11, v20
	v_sub_u32_e32 v20, v8, v19
	v_lshrrev_b32_e32 v20, 31, v20
	v_add_u32_e32 v11, v11, v20
	ds_read_b128 v[12:15], v10 offset:64
	ds_read_b128 v[16:19], v10 offset:80
	s_waitcnt lgkmcnt(0)
	v_sub_u32_e32 v20, v8, v12
	v_lshrrev_b32_e32 v20, 31, v20
	v_add_u32_e32 v11, v11, v20
	v_sub_u32_e32 v20, v8, v13
	v_lshrrev_b32_e32 v20, 31, v20
	v_add_u32_e32 v11, v11, v20
	v_sub_u32_e32 v20, v8, v14
	v_lshrrev_b32_e32 v20, 31, v20
	v_add_u32_e32 v11, v11, v20
	v_sub_u32_e32 v20, v8, v15
	v_lshrrev_b32_e32 v20, 31, v20
	v_add_u32_e32 v11, v11, v20
	v_sub_u32_e32 v20, v8, v16
	v_lshrrev_b32_e32 v20, 31, v20
	v_add_u32_e32 v11, v11, v20
	v_sub_u32_e32 v20, v8, v17
	v_lshrrev_b32_e32 v20, 31, v20
	v_add_u32_e32 v11, v11, v20
	v_sub_u32_e32 v20, v8, v18
	v_lshrrev_b32_e32 v20, 31, v20
	v_add_u32_e32 v11, v11, v20
	v_sub_u32_e32 v20, v8, v19
	v_lshrrev_b32_e32 v20, 31, v20
	v_add_u32_e32 v11, v11, v20
	ds_read_b128 v[12:15], v10 offset:96
	ds_read_b128 v[16:19], v10 offset:112
	s_waitcnt lgkmcnt(0)
	v_sub_u32_e32 v20, v8, v12
	v_lshrrev_b32_e32 v20, 31, v20
	v_add_u32_e32 v11, v11, v20
	v_sub_u32_e32 v20, v8, v13
	v_lshrrev_b32_e32 v20, 31, v20
	v_add_u32_e32 v11, v11, v20
	v_sub_u32_e32 v20, v8, v14
	v_lshrrev_b32_e32 v20, 31, v20
	v_add_u32_e32 v11, v11, v20
	v_sub_u32_e32 v20, v8, v15
	v_lshrrev_b32_e32 v20, 31, v20
	v_add_u32_e32 v11, v11, v20
	v_sub_u32_e32 v20, v8, v16
	v_lshrrev_b32_e32 v20, 31, v20
	v_add_u32_e32 v11, v11, v20
	v_sub_u32_e32 v20, v8, v17
	v_lshrrev_b32_e32 v20, 31, v20
	v_add_u32_e32 v11, v11, v20
	v_sub_u32_e32 v20, v8, v18
	v_lshrrev_b32_e32 v20, 31, v20
	v_add_u32_e32 v11, v11, v20
	v_sub_u32_e32 v20, v8, v19
	v_lshrrev_b32_e32 v20, 31, v20
	v_add_u32_e32 v11, v11, v20
	ds_read_b128 v[12:15], v10 offset:128
	ds_read_b128 v[16:19], v10 offset:144
	s_waitcnt lgkmcnt(0)
	v_sub_u32_e32 v20, v8, v12
	v_lshrrev_b32_e32 v20, 31, v20
	v_add_u32_e32 v11, v11, v20
	v_sub_u32_e32 v20, v8, v13
	v_lshrrev_b32_e32 v20, 31, v20
	v_add_u32_e32 v11, v11, v20
	v_sub_u32_e32 v20, v8, v14
	v_lshrrev_b32_e32 v20, 31, v20
	v_add_u32_e32 v11, v11, v20
	v_sub_u32_e32 v20, v8, v15
	v_lshrrev_b32_e32 v20, 31, v20
	v_add_u32_e32 v11, v11, v20
	v_sub_u32_e32 v20, v8, v16
	v_lshrrev_b32_e32 v20, 31, v20
	v_add_u32_e32 v11, v11, v20
	v_sub_u32_e32 v20, v8, v17
	v_lshrrev_b32_e32 v20, 31, v20
	v_add_u32_e32 v11, v11, v20
	v_sub_u32_e32 v20, v8, v18
	v_lshrrev_b32_e32 v20, 31, v20
	v_add_u32_e32 v11, v11, v20
	v_sub_u32_e32 v20, v8, v19
	v_lshrrev_b32_e32 v20, 31, v20
	v_add_u32_e32 v11, v11, v20
	v_cmp_gt_u32_e32 vcc, 40, v3
	s_and_saveexec_b64 s[44:45], vcc
	v_lshlrev_b32_e32 v11, 2, v11
	v_add_u32_e32 v11, s28, v11
	ds_write_b32 v11, v3 offset:6208
	s_mov_b64 exec, s[44:45]
	v_add_u32_e32 v9, s28, v2
	ds_read_b32 v12, v9 offset:6208
	ds_read_b32 v13, v9 offset:6240
	ds_read_b32 v14, v9 offset:6272
	ds_read_b32 v15, v9 offset:6304
	ds_read_b32 v16, v9 offset:6336
	s_waitcnt lgkmcnt(0)
	v_lshlrev_b32_e32 v12, 2, v12
	v_lshlrev_b32_e32 v13, 2, v13
	v_lshlrev_b32_e32 v14, 2, v14
	v_lshlrev_b32_e32 v15, 2, v15
	v_lshlrev_b32_e32 v16, 2, v16
	ds_bpermute_b32 v46, v12, v5
	ds_bpermute_b32 v51, v12, v5 offset:4
	ds_bpermute_b32 v47, v13, v5
	ds_bpermute_b32 v52, v13, v5 offset:4
	ds_bpermute_b32 v48, v14, v5
	ds_bpermute_b32 v53, v14, v5 offset:4
	ds_bpermute_b32 v49, v15, v5
	ds_bpermute_b32 v54, v15, v5 offset:4
	ds_bpermute_b32 v50, v16, v5
	ds_bpermute_b32 v55, v16, v5 offset:4
	s_waitcnt lgkmcnt(0)
	s_cmpk_gt_i32 s20, 768
	s_cbranch_scc1 .Lhq0_fallback
	s_waitcnt vmcnt(0)
	ds_write_b128 v6, v[56:59] offset:0
	ds_write_b128 v6, v[60:63] offset:1024
	ds_write_b128 v6, v[64:67] offset:2048
	ds_write_b128 v6, v[68:71] offset:3072
	ds_write_b128 v6, v[72:75] offset:4096
	ds_write_b128 v6, v[76:79] offset:5120
	s_waitcnt lgkmcnt(0)
	v_subrev_u32_e32 v46, s18, v46
	v_subrev_u32_e32 v51, s18, v51
	v_lshl_add_u32 v46, v46, 3, s28
	v_lshl_add_u32 v51, v51, 3, s28
	v_subrev_u32_e32 v47, s18, v47
	v_subrev_u32_e32 v52, s18, v52
	v_lshl_add_u32 v47, v47, 3, s28
	v_lshl_add_u32 v52, v52, 3, s28
	v_subrev_u32_e32 v48, s18, v48
	v_subrev_u32_e32 v53, s18, v53
	v_lshl_add_u32 v48, v48, 3, s28
	v_lshl_add_u32 v53, v53, 3, s28
	v_subrev_u32_e32 v49, s18, v49
	v_subrev_u32_e32 v54, s18, v54
	v_lshl_add_u32 v49, v49, 3, s28
	v_lshl_add_u32 v54, v54, 3, s28
	v_subrev_u32_e32 v50, s18, v50
	v_subrev_u32_e32 v55, s18, v55
	v_lshl_add_u32 v50, v50, 3, s28
	v_lshl_add_u32 v55, v55, 3, s28
	v_mov_b32_e32 v56, 0
	v_mov_b32_e32 v57, 0
	v_mov_b32_e32 v58, 0
	v_mov_b32_e32 v59, 0
	v_mov_b32_e32 v60, 0
	v_mov_b32_e32 v61, 0
	v_mov_b32_e32 v62, 0
	v_mov_b32_e32 v63, 0
	v_mov_b32_e32 v64, 0
	v_mov_b32_e32 v65, 0
	v_mov_b32_e32 v66, 0
	v_mov_b32_e32 v67, 0
	v_mov_b32_e32 v68, 0
	v_mov_b32_e32 v69, 0
	v_mov_b32_e32 v70, 0
	v_mov_b32_e32 v71, 0
	v_mov_b32_e32 v72, 0
	v_mov_b32_e32 v73, 0
	v_mov_b32_e32 v74, 0
	v_mov_b32_e32 v75, 0
	v_mov_b32_e32 v76, 0
	v_mov_b32_e32 v77, 0
	v_mov_b32_e32 v78, 0
	v_mov_b32_e32 v79, 0
	v_mov_b32_e32 v80, 0
	v_mov_b32_e32 v81, 0
	v_mov_b32_e32 v82, 0
	v_mov_b32_e32 v83, 0
	v_mov_b32_e32 v84, 0
	v_mov_b32_e32 v85, 0
	v_mov_b32_e32 v86, 0
	v_mov_b32_e32 v87, 0
	v_mov_b32_e32 v88, 0
	v_mov_b32_e32 v89, 0
	v_mov_b32_e32 v90, 0
	v_mov_b32_e32 v91, 0
	v_mov_b32_e32 v92, 0
	v_mov_b32_e32 v93, 0
	v_mov_b32_e32 v94, 0
	v_mov_b32_e32 v95, 0
	s_mov_b32 s27, 4

.Lhq0_epilogue:
	v_bfe_u32 v2, v0, 3, 3
	v_lshlrev_b32_e32 v2, 2, v2
	v_add_u32_e32 v2, s28, v2
	ds_read_b32 v46, v2 offset:6208
	ds_read_b32 v47, v2 offset:6240
	ds_read_b32 v48, v2 offset:6272
	ds_read_b32 v49, v2 offset:6304
	ds_read_b32 v50, v2 offset:6336
	s_waitcnt lgkmcnt(0)
	v_add_u32_e32 v46, s15, v46
	v_add_u32_e32 v47, s15, v47
	v_add_u32_e32 v48, s15, v48
	v_add_u32_e32 v49, s15, v49
	v_add_u32_e32 v50, s15, v50
	v_lshlrev_b32_e32 v51, 7, v46
	v_or_b32_e32 v51, v51, v1
	v_cvt_pk_f16_f32 v6, v56, v57
	v_cvt_pk_f16_f32 v7, v58, v59
	v_cvt_pk_f16_f32 v8, v60, v61
	v_cvt_pk_f16_f32 v9, v62, v63
	global_store_dwordx4 v51, v[6:9], s[10:11] nt
	v_lshlrev_b32_e32 v52, 7, v47
	v_or_b32_e32 v52, v52, v1
	v_cvt_pk_f16_f32 v10, v64, v65
	v_cvt_pk_f16_f32 v11, v66, v67
	v_cvt_pk_f16_f32 v12, v68, v69
	v_cvt_pk_f16_f32 v13, v70, v71
	global_store_dwordx4 v52, v[10:13], s[10:11] nt
	v_lshlrev_b32_e32 v53, 7, v48
	v_or_b32_e32 v53, v53, v1
	v_cvt_pk_f16_f32 v14, v72, v73
	v_cvt_pk_f16_f32 v15, v74, v75
	v_cvt_pk_f16_f32 v16, v76, v77
	v_cvt_pk_f16_f32 v17, v78, v79
	global_store_dwordx4 v53, v[14:17], s[10:11] nt
	v_lshlrev_b32_e32 v54, 7, v49
	v_or_b32_e32 v54, v54, v1
	v_cvt_pk_f16_f32 v18, v80, v81
	v_cvt_pk_f16_f32 v19, v82, v83
	v_cvt_pk_f16_f32 v20, v84, v85
	v_cvt_pk_f16_f32 v21, v86, v87
	global_store_dwordx4 v54, v[18:21], s[10:11] nt
	v_lshlrev_b32_e32 v55, 7, v50
	v_or_b32_e32 v55, v55, v1
	v_cvt_pk_f16_f32 v22, v88, v89
	v_cvt_pk_f16_f32 v23, v90, v91
	v_cvt_pk_f16_f32 v24, v92, v93
	v_cvt_pk_f16_f32 v25, v94, v95
	global_store_dwordx4 v55, v[22:25], s[10:11] nt

_Z5k_hopILi1EEvPKiPK15HIP_vector_typeIiLj2EEPKS2_IjLj4EEPS6_S8_S8_PKfSB_Pf:
	s_lshr_b32 s3, s2, 3
	s_cmpk_gt_u32 s3, 156
	s_cbranch_scc1 .Lhq1_exit
	s_load_dwordx4 s[4:7], s[0:1], 0x0
	s_load_dwordx4 s[8:11], s[0:1], 0x10
	s_load_dwordx4 s[48:51], s[0:1], 0x20
	s_load_dwordx4 s[52:55], s[0:1], 0x30
	s_load_dwordx2 s[56:57], s[0:1], 0x40
	v_lshrrev_b32_e32 v2, 6, v0
	v_and_b32_e32 v3, 63, v0
	s_bfe_u32 s13, s2, 0x10002
	s_and_b32 s14, s2, 3
	v_readfirstlane_b32 s12, v2
	s_lshl_b32 s15, s3, 2
	s_add_i32 s15, s15, s12
	s_mul_i32 s15, s15, 40
	s_mul_i32 s16, s14, 25000
	s_add_i32 s15, s15, s16
	s_add_i32 s16, s16, 24960
	s_min_u32 s15, s15, s16
	s_mul_i32 s17, s13, 0x61a84
	s_waitcnt lgkmcnt(0)
	s_add_u32 s4, s4, s17
	s_addc_u32 s5, s5, 0
	s_mul_i32 s17, s13, 0x927c00
	s_add_u32 s6, s6, s17
	s_addc_u32 s7, s7, 0
	s_mul_i32 s17, s13, 0xc35000
	s_add_u32 s8, s8, s17
	s_addc_u32 s9, s9, 0
	s_add_u32 s48, s48, s17
	s_addc_u32 s49, s49, 0
	s_add_u32 s50, s50, s17
	s_addc_u32 s51, s51, 0
	s_cmp_eq_u32 s13, 0
	s_cselect_b32 s58, s52, s54
	s_cselect_b32 s59, s53, s55
	s_load_dwordx4 s[52:55], s[58:59], 0x0
	s_lshl_b32 s17, s13, 8
	s_add_u32 s56, s56, s17
	s_addc_u32 s57, s57, 0
	s_mul_i32 s28, s12, 6464
	s_mov_b32 s29, 0xffff80
	v_min_u32_e32 v4, 40, v3
	v_add_u32_e32 v4, s15, v4
	v_lshlrev_b32_e32 v4, 2, v4
	global_load_dword v5, v4, s[4:5]
	v_and_b32_e32 v1, 7, v0
	v_lshlrev_b32_e32 v1, 4, v1
	v_lshrrev_b32_e32 v2, 3, v3
	v_lshlrev_b32_e32 v2, 2, v2
	v_lshlrev_b32_e32 v4, 4, v3
	v_add_u32_e32 v6, s28, v4
	v_add_u32_e32 v7, 1, v3
	v_lshlrev_b32_e32 v7, 2, v7
	s_waitcnt vmcnt(0)
	v_readlane_b32 s18, v5, 0
	v_readlane_b32 s19, v5, 40
	ds_bpermute_b32 v8, v7, v5
	s_and_b32 s18, s18, -2
	s_sub_i32 s20, s19, s18
	s_lshl_b32 s21, s18, 3
	s_add_u32 s22, s6, s21
	s_addc_u32 s23, s7, 0
	s_add_u32 s24, s22, 0x1000
	s_addc_u32 s25, s23, 0
	s_cmpk_gt_i32 s20, 768
	s_cbranch_scc1 .Lhq1_staged
	global_load_dwordx4 v[56:59], v4, s[22:23] offset:0
	s_cmpk_le_i32 s20, 128
	s_cbranch_scc1 .Lhq1_staged
	global_load_dwordx4 v[60:63], v4, s[22:23] offset:1024
	s_cmpk_le_i32 s20, 256
	s_cbranch_scc1 .Lhq1_staged
	global_load_dwordx4 v[64:67], v4, s[22:23] offset:2048
	s_cmpk_le_i32 s20, 384
	s_cbranch_scc1 .Lhq1_staged
	global_load_dwordx4 v[68:71], v4, s[22:23] offset:3072
	s_cmpk_le_i32 s20, 512
	s_cbranch_scc1 .Lhq1_staged
	global_load_dwordx4 v[72:75], v4, s[24:25] offset:0
	s_cmpk_le_i32 s20, 640
	s_cbranch_scc1 .Lhq1_staged
	global_load_dwordx4 v[76:79], v4, s[24:25] offset:1024

.Lhq1_epilogue:
	v_bfe_u32 v2, v0, 3, 3
	v_lshlrev_b32_e32 v2, 2, v2
	v_add_u32_e32 v2, s28, v2
	ds_read_b32 v46, v2 offset:6208
	ds_read_b32 v47, v2 offset:6240
	ds_read_b32 v48, v2 offset:6272
	ds_read_b32 v49, v2 offset:6304
	ds_read_b32 v50, v2 offset:6336
	s_waitcnt lgkmcnt(0)
	v_add_u32_e32 v46, s15, v46
	v_add_u32_e32 v47, s15, v47
	v_add_u32_e32 v48, s15, v48
	v_add_u32_e32 v49, s15, v49
	v_add_u32_e32 v50, s15, v50
	s_mov_b32 s46, s55
	v_lshlrev_b32_e32 v3, 7, v46
	v_or_b32_e32 v3, v3, v1
	global_load_dwordx4 v[6:9], v3, s[48:49] nt
	global_load_dwordx4 v[10:13], v3, s[50:51] nt
	global_load_dwordx4 v[14:17], v3, s[8:9]
	v_lshlrev_b32_e32 v4, 7, v47
	v_or_b32_e32 v4, v4, v1
	global_load_dwordx4 v[18:21], v4, s[48:49] nt
	global_load_dwordx4 v[22:25], v4, s[50:51] nt
	global_load_dwordx4 v[26:29], v4, s[8:9]
	s_waitcnt vmcnt(3)
	v_cvt_f32_f16_e32 v38, v6
	v_cvt_f32_f16_sdwa v39, v6 dst_sel:DWORD dst_unused:UNUSED_PAD src0_sel:WORD_1
	v_cvt_f32_f16_e32 v40, v8
	v_cvt_f32_f16_sdwa v41, v8 dst_sel:DWORD dst_unused:UNUSED_PAD src0_sel:WORD_1
	v_cvt_f32_f16_e32 v6, v7
	v_cvt_f32_f16_sdwa v7, v7 dst_sel:DWORD dst_unused:UNUSED_PAD src0_sel:WORD_1
	v_cvt_f32_f16_e32 v8, v9
	v_cvt_f32_f16_sdwa v9, v9 dst_sel:DWORD dst_unused:UNUSED_PAD src0_sel:WORD_1
	v_mul_f32_e32 v30, s52, v38
	v_mul_f32_e32 v31, s52, v39
	v_mul_f32_e32 v32, s52, v6
	v_mul_f32_e32 v33, s52, v7
	v_mul_f32_e32 v34, s52, v40
	v_mul_f32_e32 v35, s52, v41
	v_mul_f32_e32 v36, s52, v8
	v_mul_f32_e32 v37, s52, v9
	v_cvt_f32_f16_e32 v38, v10
	v_cvt_f32_f16_sdwa v39, v10 dst_sel:DWORD dst_unused:UNUSED_PAD src0_sel:WORD_1
	v_cvt_f32_f16_e32 v40, v12
	v_cvt_f32_f16_sdwa v41, v12 dst_sel:DWORD dst_unused:UNUSED_PAD src0_sel:WORD_1
	v_cvt_f32_f16_e32 v10, v11
	v_cvt_f32_f16_sdwa v11, v11 dst_sel:DWORD dst_unused:UNUSED_PAD src0_sel:WORD_1
	v_cvt_f32_f16_e32 v12, v13
	v_cvt_f32_f16_sdwa v13, v13 dst_sel:DWORD dst_unused:UNUSED_PAD src0_sel:WORD_1
	v_fma_f32 v30, s53, v38, v30
	v_fma_f32 v31, s53, v39, v31
	v_fma_f32 v32, s53, v10, v32
	v_fma_f32 v33, s53, v11, v33
	v_fma_f32 v34, s53, v40, v34
	v_fma_f32 v35, s53, v41, v35
	v_fma_f32 v36, s53, v12, v36
	v_fma_f32 v37, s53, v13, v37
	v_cvt_f32_f16_e32 v38, v14
	v_cvt_f32_f16_sdwa v39, v14 dst_sel:DWORD dst_unused:UNUSED_PAD src0_sel:WORD_1
	v_cvt_f32_f16_e32 v40, v16
	v_cvt_f32_f16_sdwa v41, v16 dst_sel:DWORD dst_unused:UNUSED_PAD src0_sel:WORD_1
	v_cvt_f32_f16_e32 v14, v15
	v_cvt_f32_f16_sdwa v15, v15 dst_sel:DWORD dst_unused:UNUSED_PAD src0_sel:WORD_1
	v_cvt_f32_f16_e32 v16, v17
	v_cvt_f32_f16_sdwa v17, v17 dst_sel:DWORD dst_unused:UNUSED_PAD src0_sel:WORD_1
	v_fma_f32 v30, s54, v38, v30
	v_fma_f32 v31, s54, v39, v31
	v_fma_f32 v32, s54, v14, v32
	v_fma_f32 v33, s54, v15, v33
	v_fma_f32 v34, s54, v40, v34
	v_fma_f32 v35, s54, v41, v35
	v_fma_f32 v36, s54, v16, v36
	v_fma_f32 v37, s54, v17, v37
	v_fma_f32 v30, s46, v56, v30
	v_fma_f32 v31, s46, v57, v31
	v_fma_f32 v32, s46, v58, v32
	v_fma_f32 v33, s46, v59, v33
	v_fma_f32 v34, s46, v60, v34
	v_fma_f32 v35, s46, v61, v35
	v_fma_f32 v36, s46, v62, v36
	v_fma_f32 v37, s46, v63, v37
	v_lshlrev_b32_e32 v46, 9, v46
	v_or_b32_e32 v46, v46, v1
	global_store_dwordx4 v46, v[30:33], s[56:57] nt
	global_store_dwordx4 v46, v[34:37], s[56:57] offset:128 nt
	v_lshlrev_b32_e32 v3, 7, v48
	v_or_b32_e32 v3, v3, v1
	global_load_dwordx4 v[6:9], v3, s[48:49] nt
	global_load_dwordx4 v[10:13], v3, s[50:51] nt
	global_load_dwordx4 v[14:17], v3, s[8:9]
	s_waitcnt vmcnt(5)
	v_cvt_f32_f16_e32 v38, v18
	v_cvt_f32_f16_sdwa v39, v18 dst_sel:DWORD dst_unused:UNUSED_PAD src0_sel:WORD_1
	v_cvt_f32_f16_e32 v40, v20
	v_cvt_f32_f16_sdwa v41, v20 dst_sel:DWORD dst_unused:UNUSED_PAD src0_sel:WORD_1
	v_cvt_f32_f16_e32 v18, v19
	v_cvt_f32_f16_sdwa v19, v19 dst_sel:DWORD dst_unused:UNUSED_PAD src0_sel:WORD_1
	v_cvt_f32_f16_e32 v20, v21
	v_cvt_f32_f16_sdwa v21, v21 dst_sel:DWORD dst_unused:UNUSED_PAD src0_sel:WORD_1
	v_mul_f32_e32 v30, s52, v38
	v_mul_f32_e32 v31, s52, v39
	v_mul_f32_e32 v32, s52, v18
	v_mul_f32_e32 v33, s52, v19
	v_mul_f32_e32 v34, s52, v40
	v_mul_f32_e32 v35, s52, v41
	v_mul_f32_e32 v36, s52, v20
	v_mul_f32_e32 v37, s52, v21
	v_cvt_f32_f16_e32 v38, v22
	v_cvt_f32_f16_sdwa v39, v22 dst_sel:DWORD dst_unused:UNUSED_PAD src0_sel:WORD_1
	v_cvt_f32_f16_e32 v40, v24
	v_cvt_f32_f16_sdwa v41, v24 dst_sel:DWORD dst_unused:UNUSED_PAD src0_sel:WORD_1
	v_cvt_f32_f16_e32 v22, v23
	v_cvt_f32_f16_sdwa v23, v23 dst_sel:DWORD dst_unused:UNUSED_PAD src0_sel:WORD_1
	v_cvt_f32_f16_e32 v24, v25
	v_cvt_f32_f16_sdwa v25, v25 dst_sel:DWORD dst_unused:UNUSED_PAD src0_sel:WORD_1
	v_fma_f32 v30, s53, v38, v30
	v_fma_f32 v31, s53, v39, v31
	v_fma_f32 v32, s53, v22, v32
	v_fma_f32 v33, s53, v23, v33
	v_fma_f32 v34, s53, v40, v34
	v_fma_f32 v35, s53, v41, v35
	v_fma_f32 v36, s53, v24, v36
	v_fma_f32 v37, s53, v25, v37
	v_cvt_f32_f16_e32 v38, v26
	v_cvt_f32_f16_sdwa v39, v26 dst_sel:DWORD dst_unused:UNUSED_PAD src0_sel:WORD_1
	v_cvt_f32_f16_e32 v40, v28
	v_cvt_f32_f16_sdwa v41, v28 dst_sel:DWORD dst_unused:UNUSED_PAD src0_sel:WORD_1
	v_cvt_f32_f16_e32 v26, v27
	v_cvt_f32_f16_sdwa v27, v27 dst_sel:DWORD dst_unused:UNUSED_PAD src0_sel:WORD_1
	v_cvt_f32_f16_e32 v28, v29
	v_cvt_f32_f16_sdwa v29, v29 dst_sel:DWORD dst_unused:UNUSED_PAD src0_sel:WORD_1
	v_fma_f32 v30, s54, v38, v30
	v_fma_f32 v31, s54, v39, v31
	v_fma_f32 v32, s54, v26, v32
	v_fma_f32 v33, s54, v27, v33
	v_fma_f32 v34, s54, v40, v34
	v_fma_f32 v35, s54, v41, v35
	v_fma_f32 v36, s54, v28, v36
	v_fma_f32 v37, s54, v29, v37
	v_fma_f32 v30, s46, v64, v30
	v_fma_f32 v31, s46, v65, v31
	v_fma_f32 v32, s46, v66, v32
	v_fma_f32 v33, s46, v67, v33
	v_fma_f32 v34, s46, v68, v34
	v_fma_f32 v35, s46, v69, v35
	v_fma_f32 v36, s46, v70, v36
	v_fma_f32 v37, s46, v71, v37
	v_lshlrev_b32_e32 v47, 9, v47
	v_or_b32_e32 v47, v47, v1
	global_store_dwordx4 v47, v[30:33], s[56:57] nt
	global_store_dwordx4 v47, v[34:37], s[56:57] offset:128 nt
	v_lshlrev_b32_e32 v4, 7, v49
	v_or_b32_e32 v4, v4, v1
	global_load_dwordx4 v[18:21], v4, s[48:49] nt
	global_load_dwordx4 v[22:25], v4, s[50:51] nt
	global_load_dwordx4 v[26:29], v4, s[8:9]
	s_waitcnt vmcnt(5)
	v_cvt_f32_f16_e32 v38, v6
	v_cvt_f32_f16_sdwa v39, v6 dst_sel:DWORD dst_unused:UNUSED_PAD src0_sel:WORD_1
	v_cvt_f32_f16_e32 v40, v8
	v_cvt_f32_f16_sdwa v41, v8 dst_sel:DWORD dst_unused:UNUSED_PAD src0_sel:WORD_1
	v_cvt_f32_f16_e32 v6, v7
	v_cvt_f32_f16_sdwa v7, v7 dst_sel:DWORD dst_unused:UNUSED_PAD src0_sel:WORD_1
	v_cvt_f32_f16_e32 v8, v9
	v_cvt_f32_f16_sdwa v9, v9 dst_sel:DWORD dst_unused:UNUSED_PAD src0_sel:WORD_1
	v_mul_f32_e32 v30, s52, v38
	v_mul_f32_e32 v31, s52, v39
	v_mul_f32_e32 v32, s52, v6
	v_mul_f32_e32 v33, s52, v7
	v_mul_f32_e32 v34, s52, v40
	v_mul_f32_e32 v35, s52, v41
	v_mul_f32_e32 v36, s52, v8
	v_mul_f32_e32 v37, s52, v9
	v_cvt_f32_f16_e32 v38, v10
	v_cvt_f32_f16_sdwa v39, v10 dst_sel:DWORD dst_unused:UNUSED_PAD src0_sel:WORD_1
	v_cvt_f32_f16_e32 v40, v12
	v_cvt_f32_f16_sdwa v41, v12 dst_sel:DWORD dst_unused:UNUSED_PAD src0_sel:WORD_1
	v_cvt_f32_f16_e32 v10, v11
	v_cvt_f32_f16_sdwa v11, v11 dst_sel:DWORD dst_unused:UNUSED_PAD src0_sel:WORD_1
	v_cvt_f32_f16_e32 v12, v13
	v_cvt_f32_f16_sdwa v13, v13 dst_sel:DWORD dst_unused:UNUSED_PAD src0_sel:WORD_1
	v_fma_f32 v30, s53, v38, v30
	v_fma_f32 v31, s53, v39, v31
	v_fma_f32 v32, s53, v10, v32
	v_fma_f32 v33, s53, v11, v33
	v_fma_f32 v34, s53, v40, v34
	v_fma_f32 v35, s53, v41, v35
	v_fma_f32 v36, s53, v12, v36
	v_fma_f32 v37, s53, v13, v37
	v_cvt_f32_f16_e32 v38, v14
	v_cvt_f32_f16_sdwa v39, v14 dst_sel:DWORD dst_unused:UNUSED_PAD src0_sel:WORD_1
	v_cvt_f32_f16_e32 v40, v16
	v_cvt_f32_f16_sdwa v41, v16 dst_sel:DWORD dst_unused:UNUSED_PAD src0_sel:WORD_1
	v_cvt_f32_f16_e32 v14, v15
	v_cvt_f32_f16_sdwa v15, v15 dst_sel:DWORD dst_unused:UNUSED_PAD src0_sel:WORD_1
	v_cvt_f32_f16_e32 v16, v17
	v_cvt_f32_f16_sdwa v17, v17 dst_sel:DWORD dst_unused:UNUSED_PAD src0_sel:WORD_1
	v_fma_f32 v30, s54, v38, v30
	v_fma_f32 v31, s54, v39, v31
	v_fma_f32 v32, s54, v14, v32
	v_fma_f32 v33, s54, v15, v33
	v_fma_f32 v34, s54, v40, v34
	v_fma_f32 v35, s54, v41, v35
	v_fma_f32 v36, s54, v16, v36
	v_fma_f32 v37, s54, v17, v37
	v_fma_f32 v30, s46, v72, v30
	v_fma_f32 v31, s46, v73, v31
	v_fma_f32 v32, s46, v74, v32
	v_fma_f32 v33, s46, v75, v33
	v_fma_f32 v34, s46, v76, v34
	v_fma_f32 v35, s46, v77, v35
	v_fma_f32 v36, s46, v78, v36
	v_fma_f32 v37, s46, v79, v37
	v_lshlrev_b32_e32 v48, 9, v48
	v_or_b32_e32 v48, v48, v1
	global_store_dwordx4 v48, v[30:33], s[56:57] nt
	global_store_dwordx4 v48, v[34:37], s[56:57] offset:128 nt
	v_lshlrev_b32_e32 v3, 7, v50
	v_or_b32_e32 v3, v3, v1
	global_load_dwordx4 v[6:9], v3, s[48:49] nt
	global_load_dwordx4 v[10:13], v3, s[50:51] nt
	global_load_dwordx4 v[14:17], v3, s[8:9]
	s_waitcnt vmcnt(5)
	v_cvt_f32_f16_e32 v38, v18
	v_cvt_f32_f16_sdwa v39, v18 dst_sel:DWORD dst_unused:UNUSED_PAD src0_sel:WORD_1
	v_cvt_f32_f16_e32 v40, v20
	v_cvt_f32_f16_sdwa v41, v20 dst_sel:DWORD dst_unused:UNUSED_PAD src0_sel:WORD_1
	v_cvt_f32_f16_e32 v18, v19
	v_cvt_f32_f16_sdwa v19, v19 dst_sel:DWORD dst_unused:UNUSED_PAD src0_sel:WORD_1
	v_cvt_f32_f16_e32 v20, v21
	v_cvt_f32_f16_sdwa v21, v21 dst_sel:DWORD dst_unused:UNUSED_PAD src0_sel:WORD_1
	v_mul_f32_e32 v30, s52, v38
	v_mul_f32_e32 v31, s52, v39
	v_mul_f32_e32 v32, s52, v18
	v_mul_f32_e32 v33, s52, v19
	v_mul_f32_e32 v34, s52, v40
	v_mul_f32_e32 v35, s52, v41
	v_mul_f32_e32 v36, s52, v20
	v_mul_f32_e32 v37, s52, v21
	v_cvt_f32_f16_e32 v38, v22
	v_cvt_f32_f16_sdwa v39, v22 dst_sel:DWORD dst_unused:UNUSED_PAD src0_sel:WORD_1
	v_cvt_f32_f16_e32 v40, v24
	v_cvt_f32_f16_sdwa v41, v24 dst_sel:DWORD dst_unused:UNUSED_PAD src0_sel:WORD_1
	v_cvt_f32_f16_e32 v22, v23
	v_cvt_f32_f16_sdwa v23, v23 dst_sel:DWORD dst_unused:UNUSED_PAD src0_sel:WORD_1
	v_cvt_f32_f16_e32 v24, v25
	v_cvt_f32_f16_sdwa v25, v25 dst_sel:DWORD dst_unused:UNUSED_PAD src0_sel:WORD_1
	v_fma_f32 v30, s53, v38, v30
	v_fma_f32 v31, s53, v39, v31
	v_fma_f32 v32, s53, v22, v32
	v_fma_f32 v33, s53, v23, v33
	v_fma_f32 v34, s53, v40, v34
	v_fma_f32 v35, s53, v41, v35
	v_fma_f32 v36, s53, v24, v36
	v_fma_f32 v37, s53, v25, v37
	v_cvt_f32_f16_e32 v38, v26
	v_cvt_f32_f16_sdwa v39, v26 dst_sel:DWORD dst_unused:UNUSED_PAD src0_sel:WORD_1
	v_cvt_f32_f16_e32 v40, v28
	v_cvt_f32_f16_sdwa v41, v28 dst_sel:DWORD dst_unused:UNUSED_PAD src0_sel:WORD_1
	v_cvt_f32_f16_e32 v26, v27
	v_cvt_f32_f16_sdwa v27, v27 dst_sel:DWORD dst_unused:UNUSED_PAD src0_sel:WORD_1
	v_cvt_f32_f16_e32 v28, v29
	v_cvt_f32_f16_sdwa v29, v29 dst_sel:DWORD dst_unused:UNUSED_PAD src0_sel:WORD_1
	v_fma_f32 v30, s54, v38, v30
	v_fma_f32 v31, s54, v39, v31
	v_fma_f32 v32, s54, v26, v32
	v_fma_f32 v33, s54, v27, v33
	v_fma_f32 v34, s54, v40, v34
	v_fma_f32 v35, s54, v41, v35
	v_fma_f32 v36, s54, v28, v36
	v_fma_f32 v37, s54, v29, v37
	v_fma_f32 v30, s46, v80, v30
	v_fma_f32 v31, s46, v81, v31
	v_fma_f32 v32, s46, v82, v32
	v_fma_f32 v33, s46, v83, v33
	v_fma_f32 v34, s46, v84, v34
	v_fma_f32 v35, s46, v85, v35
	v_fma_f32 v36, s46, v86, v36
	v_fma_f32 v37, s46, v87, v37
	v_lshlrev_b32_e32 v49, 9, v49
	v_or_b32_e32 v49, v49, v1
	global_store_dwordx4 v49, v[30:33], s[56:57] nt
	global_store_dwordx4 v49, v[34:37], s[56:57] offset:128 nt
	s_waitcnt vmcnt(2)
	v_cvt_f32_f16_e32 v38, v6
	v_cvt_f32_f16_sdwa v39, v6 dst_sel:DWORD dst_unused:UNUSED_PAD src0_sel:WORD_1
	v_cvt_f32_f16_e32 v40, v8
	v_cvt_f32_f16_sdwa v41, v8 dst_sel:DWORD dst_unused:UNUSED_PAD src0_sel:WORD_1
	v_cvt_f32_f16_e32 v6, v7
	v_cvt_f32_f16_sdwa v7, v7 dst_sel:DWORD dst_unused:UNUSED_PAD src0_sel:WORD_1
	v_cvt_f32_f16_e32 v8, v9
	v_cvt_f32_f16_sdwa v9, v9 dst_sel:DWORD dst_unused:UNUSED_PAD src0_sel:WORD_1
	v_mul_f32_e32 v30, s52, v38
	v_mul_f32_e32 v31, s52, v39
	v_mul_f32_e32 v32, s52, v6
	v_mul_f32_e32 v33, s52, v7
	v_mul_f32_e32 v34, s52, v40
	v_mul_f32_e32 v35, s52, v41
	v_mul_f32_e32 v36, s52, v8
	v_mul_f32_e32 v37, s52, v9
	v_cvt_f32_f16_e32 v38, v10
	v_cvt_f32_f16_sdwa v39, v10 dst_sel:DWORD dst_unused:UNUSED_PAD src0_sel:WORD_1
	v_cvt_f32_f16_e32 v40, v12
	v_cvt_f32_f16_sdwa v41, v12 dst_sel:DWORD dst_unused:UNUSED_PAD src0_sel:WORD_1
	v_cvt_f32_f16_e32 v10, v11
	v_cvt_f32_f16_sdwa v11, v11 dst_sel:DWORD dst_unused:UNUSED_PAD src0_sel:WORD_1
	v_cvt_f32_f16_e32 v12, v13
	v_cvt_f32_f16_sdwa v13, v13 dst_sel:DWORD dst_unused:UNUSED_PAD src0_sel:WORD_1
	v_fma_f32 v30, s53, v38, v30
	v_fma_f32 v31, s53, v39, v31
	v_fma_f32 v32, s53, v10, v32
	v_fma_f32 v33, s53, v11, v33
	v_fma_f32 v34, s53, v40, v34
	v_fma_f32 v35, s53, v41, v35
	v_fma_f32 v36, s53, v12, v36
	v_fma_f32 v37, s53, v13, v37
	v_cvt_f32_f16_e32 v38, v14
	v_cvt_f32_f16_sdwa v39, v14 dst_sel:DWORD dst_unused:UNUSED_PAD src0_sel:WORD_1
	v_cvt_f32_f16_e32 v40, v16
	v_cvt_f32_f16_sdwa v41, v16 dst_sel:DWORD dst_unused:UNUSED_PAD src0_sel:WORD_1
	v_cvt_f32_f16_e32 v14, v15
	v_cvt_f32_f16_sdwa v15, v15 dst_sel:DWORD dst_unused:UNUSED_PAD src0_sel:WORD_1
	v_cvt_f32_f16_e32 v16, v17
	v_cvt_f32_f16_sdwa v17, v17 dst_sel:DWORD dst_unused:UNUSED_PAD src0_sel:WORD_1
	v_fma_f32 v30, s54, v38, v30
	v_fma_f32 v31, s54, v39, v31
	v_fma_f32 v32, s54, v14, v32
	v_fma_f32 v33, s54, v15, v33
	v_fma_f32 v34, s54, v40, v34
	v_fma_f32 v35, s54, v41, v35
	v_fma_f32 v36, s54, v16, v36
	v_fma_f32 v37, s54, v17, v37
	v_fma_f32 v30, s46, v88, v30
	v_fma_f32 v31, s46, v89, v31
	v_fma_f32 v32, s46, v90, v32
	v_fma_f32 v33, s46, v91, v33
	v_fma_f32 v34, s46, v92, v34
	v_fma_f32 v35, s46, v93, v35
	v_fma_f32 v36, s46, v94, v36
	v_fma_f32 v37, s46, v95, v37
	v_lshlrev_b32_e32 v50, 9, v50
	v_or_b32_e32 v50, v50, v1
	global_store_dwordx4 v50, v[30:33], s[56:57] nt
	global_store_dwordx4 v50, v[34:37], s[56:57] offset:128 nt
